# barrier A waits lgkmcnt(2) (wave-private waf writes may stay in flight); dropped redundant s_nop in QK blocks
# speedup vs baseline: 1.0121x; 1.0121x over previous
.LBB1_10:
	ds_read_b128 v[4:7], v226 offset:384
	ds_read_b128 v[8:11], v226 offset:400
	ds_read_b128 v[12:15], v206 offset:38912
	ds_read_b128 v[82:85], v226 offset:416
	ds_read_b128 v[86:89], v226 offset:432
	s_waitcnt lgkmcnt(3)
	v_fma_mix_f32 v18, v162, s42, v4 op_sel:[0,0,0] op_sel_hi:[1,0,0]
	v_fma_mix_f32 v19, v162, s42, v5 op_sel:[1,0,0] op_sel_hi:[1,0,0]
	v_fma_mix_f32 v20, v163, s42, v6 op_sel:[0,0,0] op_sel_hi:[1,0,0]
	v_fma_mix_f32 v21, v163, s42, v7 op_sel:[1,0,0] op_sel_hi:[1,0,0]
	v_fma_mix_f32 v22, v164, s42, v8 op_sel:[0,0,0] op_sel_hi:[1,0,0]
	v_fma_mix_f32 v23, v164, s42, v9 op_sel:[1,0,0] op_sel_hi:[1,0,0]
	v_fma_mix_f32 v24, v165, s42, v10 op_sel:[0,0,0] op_sel_hi:[1,0,0]
	v_fma_mix_f32 v25, v165, s42, v11 op_sel:[1,0,0] op_sel_hi:[1,0,0]
	ds_read_b128 v[4:7], v206 offset:39936
	s_waitcnt lgkmcnt(1)
	v_fma_mix_f32 v26, v166, s42, v82 op_sel:[0,0,0] op_sel_hi:[1,0,0]
	v_fma_mix_f32 v27, v166, s42, v83 op_sel:[1,0,0] op_sel_hi:[1,0,0]
	v_fma_mix_f32 v28, v167, s42, v84 op_sel:[0,0,0] op_sel_hi:[1,0,0]
	v_fma_mix_f32 v29, v167, s42, v85 op_sel:[1,0,0] op_sel_hi:[1,0,0]
	v_fma_mix_f32 v30, v168, s42, v86 op_sel:[0,0,0] op_sel_hi:[1,0,0]
	v_fma_mix_f32 v31, v168, s42, v87 op_sel:[1,0,0] op_sel_hi:[1,0,0]
	v_fma_mix_f32 v32, v169, s42, v88 op_sel:[0,0,0] op_sel_hi:[1,0,0]
	v_fma_mix_f32 v33, v169, s42, v89 op_sel:[1,0,0] op_sel_hi:[1,0,0]
	s_nop 1
	s_nop 0
	v_mfma_f32_32x32x16_f16 v[18:33], v[12:15], v[198:201], v[18:33]
	s_waitcnt lgkmcnt(0)
	v_mfma_f32_32x32x16_f16 v[18:33], v[4:7], v[202:205], v[18:33]

.LBB1_59:
	s_setprio 0
	s_nop 10
	v_rcp_f32_e32 v8, v82
	v_cvt_f32_f16_sdwa v5, v229 dst_sel:DWORD dst_unused:UNUSED_PAD src0_sel:WORD_1
	v_cvt_f32_f16_e32 v4, v229
	v_cvt_f32_f16_sdwa v7, v230 dst_sel:DWORD dst_unused:UNUSED_PAD src0_sel:WORD_1
	v_cvt_f32_f16_e32 v6, v230
	v_cvt_f32_f16_sdwa v11, v232 dst_sel:DWORD dst_unused:UNUSED_PAD src0_sel:WORD_1
	v_cvt_f32_f16_e32 v10, v232
	v_cvt_f32_f16_sdwa v13, v234 dst_sel:DWORD dst_unused:UNUSED_PAD src0_sel:WORD_1
	v_cvt_f32_f16_e32 v12, v234
	v_pk_mul_f32 v[4:5], v[8:9], v[4:5] op_sel_hi:[0,1]
	v_pk_mul_f32 v[6:7], v[8:9], v[6:7] op_sel_hi:[0,1]
	v_pk_mul_f32 v[4:5], v[98:99], v[4:5]
	v_pk_mul_f32 v[6:7], v[100:101], v[6:7]
	v_cvt_pk_f16_f32 v4, v4, v5
	v_cvt_pk_f16_f32 v5, v6, v7
	v_pk_mul_f32 v[6:7], v[8:9], v[10:11] op_sel_hi:[0,1]
	v_pk_mul_f32 v[10:11], v[8:9], v[12:13] op_sel_hi:[0,1]
	v_pk_mul_f32 v[6:7], v[102:103], v[6:7]
	v_pk_mul_f32 v[10:11], v[104:105], v[10:11]
	v_cvt_pk_f16_f32 v6, v6, v7
	v_cvt_pk_f16_f32 v7, v10, v11
	v_cvt_f32_f16_sdwa v11, v228 dst_sel:DWORD dst_unused:UNUSED_PAD src0_sel:WORD_1
	v_cvt_f32_f16_e32 v10, v228
	ds_write_b128 v227, v[4:7]
	v_cvt_f32_f16_sdwa v7, v231 dst_sel:DWORD dst_unused:UNUSED_PAD src0_sel:WORD_1
	v_cvt_f32_f16_e32 v6, v231
	v_pk_mul_f32 v[4:5], v[8:9], v[10:11] op_sel_hi:[0,1]
	v_cvt_f32_f16_sdwa v11, v233 dst_sel:DWORD dst_unused:UNUSED_PAD src0_sel:WORD_1
	v_cvt_f32_f16_e32 v10, v233
	v_cvt_f32_f16_sdwa v13, v235 dst_sel:DWORD dst_unused:UNUSED_PAD src0_sel:WORD_1
	v_cvt_f32_f16_e32 v12, v235
	v_pk_mul_f32 v[6:7], v[8:9], v[6:7] op_sel_hi:[0,1]
	v_pk_mul_f32 v[4:5], v[4:5], v[106:107]
	v_pk_mul_f32 v[6:7], v[6:7], v[108:109]
	v_cvt_pk_f16_f32 v4, v4, v5
	v_cvt_pk_f16_f32 v5, v6, v7
	v_pk_mul_f32 v[6:7], v[8:9], v[10:11] op_sel_hi:[0,1]
	v_pk_mul_f32 v[8:9], v[8:9], v[12:13] op_sel_hi:[0,1]
	v_pk_mul_f32 v[6:7], v[6:7], v[110:111]
	v_pk_mul_f32 v[8:9], v[8:9], v[112:113]
	v_cvt_pk_f16_f32 v6, v6, v7
	v_cvt_pk_f16_f32 v7, v8, v9
	s_and_b64 vcc, exec, s[16:17]
	ds_write_b128 v227, v[4:7] offset:1024
	s_waitcnt vmcnt(0) lgkmcnt(2)
	s_barrier
	s_cbranch_vccnz .LBB1_5
	ds_read_b128 v[4:7], v206 offset:8192
	ds_read_b128 v[8:11], v206 offset:9216
	s_waitcnt lgkmcnt(1)
	v_mfma_f32_32x32x16_f16 v[114:129], v[4:7], v[130:133], 0
	ds_read_b128 v[4:7], v206 offset:16384
	ds_read_b128 v[12:15], v206 offset:17408
	s_waitcnt lgkmcnt(1)
	v_mfma_f32_32x32x16_f16 v[98:113], v[130:133], v[4:7], 0
	v_mfma_f32_32x32x16_f16 v[114:129], v[8:11], v[134:137], v[114:129]
	ds_read_b128 v[4:7], v206 offset:10240
	ds_read_b128 v[8:11], v206 offset:11264
	s_waitcnt lgkmcnt(2)
	v_mfma_f32_32x32x16_f16 v[98:113], v[134:137], v[12:15], v[98:113]
	s_waitcnt lgkmcnt(1)
	v_mfma_f32_32x32x16_f16 v[114:129], v[4:7], v[138:141], v[114:129]
	ds_read_b128 v[4:7], v206 offset:18432
	ds_read_b128 v[12:15], v206 offset:19456
	s_waitcnt lgkmcnt(1)
	v_mfma_f32_32x32x16_f16 v[98:113], v[138:141], v[4:7], v[98:113]
	v_mfma_f32_32x32x16_f16 v[114:129], v[8:11], v[142:145], v[114:129]
	ds_read_b128 v[4:7], v206 offset:12288
	ds_read_b128 v[8:11], v206 offset:13312
	s_waitcnt lgkmcnt(2)
	v_mfma_f32_32x32x16_f16 v[98:113], v[142:145], v[12:15], v[98:113]
	s_waitcnt lgkmcnt(1)
	v_mfma_f32_32x32x16_f16 v[114:129], v[4:7], v[146:149], v[114:129]
	ds_read_b128 v[4:7], v206 offset:20480
	ds_read_b128 v[12:15], v206 offset:21504
	s_waitcnt lgkmcnt(1)
	v_mfma_f32_32x32x16_f16 v[98:113], v[146:149], v[4:7], v[98:113]
	v_mfma_f32_32x32x16_f16 v[114:129], v[8:11], v[150:153], v[114:129]
	ds_read_b128 v[4:7], v206 offset:14336
	ds_read_b128 v[8:11], v206 offset:15360
	s_waitcnt lgkmcnt(2)
	v_mfma_f32_32x32x16_f16 v[98:113], v[150:153], v[12:15], v[98:113]
	s_waitcnt lgkmcnt(1)
	v_mfma_f32_32x32x16_f16 v[114:129], v[4:7], v[154:157], v[114:129]
	ds_read_b128 v[4:7], v206 offset:22528
	ds_read_b128 v[12:15], v206 offset:23552
	s_waitcnt lgkmcnt(1)
	v_mfma_f32_32x32x16_f16 v[98:113], v[154:157], v[4:7], v[98:113]
	v_mfma_f32_32x32x16_f16 v[114:129], v[8:11], v[158:161], v[114:129]
	ds_read_b128 v[4:7], v206 offset:24576
	ds_read_b128 v[8:11], v206 offset:25600
	s_waitcnt lgkmcnt(1)
	v_mfma_f32_32x32x16_f16 v[82:97], v[4:7], v[130:133], 0
	global_load_dwordx4 v[4:7], v[220:221], off
	s_nop 6
	v_cvt_pk_f16_f32 v121, v120, v121
	v_cvt_pk_f16_f32 v120, v118, v119
	v_cvt_pk_f16_f32 v119, v116, v117
	v_cvt_pk_f16_f32 v118, v114, v115
	v_cvt_pk_f16_f32 v117, v128, v129
	v_cvt_pk_f16_f32 v116, v126, v127
	s_waitcnt lgkmcnt(0)
	v_mfma_f32_32x32x16_f16 v[82:97], v[8:11], v[134:137], v[82:97]
	v_cvt_pk_f16_f32 v115, v124, v125
	v_cvt_pk_f16_f32 v114, v122, v123
	v_mfma_f32_32x32x16_f16 v[98:113], v[158:161], v[12:15], v[98:113]
	ds_read_b128 v[8:11], v206 offset:26624
	ds_read_b128 v[12:15], v206 offset:27648
	ds_read_b128 v[196:199], v206 offset:28672
	ds_write_b128 v209, v[114:117] offset:33792
	global_load_dwordx4 v[114:117], v[220:221], off offset:96
	ds_write_b128 v209, v[118:121] offset:32768
	ds_read_b128 v[118:121], v206 offset:29696
	s_nop 4
	v_cvt_pk_f16_f32 v105, v104, v105
	s_waitcnt lgkmcnt(5)
	v_mfma_f32_32x32x16_f16 v[82:97], v[8:11], v[138:141], v[82:97]
	global_load_dwordx4 v[8:11], v[220:221], off offset:32
	v_cvt_pk_f16_f32 v104, v102, v103
	v_cvt_pk_f16_f32 v103, v100, v101
	v_cvt_pk_f16_f32 v102, v98, v99
	ds_read_b128 v[98:101], v206 offset:30720
	ds_write_b128 v209, v[102:105] offset:49152
	v_cvt_pk_f16_f32 v103, v108, v109
	s_waitcnt lgkmcnt(6)
	v_mfma_f32_32x32x16_f16 v[82:97], v[12:15], v[142:145], v[82:97]
	global_load_dwordx4 v[12:15], v[220:221], off offset:64
	v_cvt_pk_f16_f32 v102, v106, v107
	ds_read_b128 v[106:109], v206 offset:31744
	v_cvt_pk_f16_f32 v105, v112, v113
	v_cvt_pk_f16_f32 v104, v110, v111
	ds_write_b128 v209, v[102:105] offset:50176
	s_waitcnt lgkmcnt(7)
	v_mfma_f32_32x32x16_f16 v[82:97], v[196:199], v[146:149], v[82:97]
	s_waitcnt lgkmcnt(4)
	v_mfma_f32_32x32x16_f16 v[82:97], v[118:121], v[150:153], v[82:97]
	s_waitcnt lgkmcnt(3)
	v_mfma_f32_32x32x16_f16 v[82:97], v[98:101], v[154:157], v[82:97]
	ds_read_b128 v[98:101], v206
	ds_read_b128 v[118:121], v206 offset:1024
	ds_read_b128 v[122:125], v206 offset:2048
	ds_read_b128 v[126:129], v206 offset:3072
	ds_read_b128 v[196:199], v206 offset:4096
	ds_read_b128 v[200:203], v206 offset:5120
	ds_read_b128 v[230:233], v206 offset:6144
	ds_read_b128 v[236:239], v206 offset:7168
	s_waitcnt lgkmcnt(0)
	s_barrier
	v_mfma_f32_32x32x16_f16 v[82:97], v[106:109], v[158:161], v[82:97]
	v_mfma_f32_32x32x16_f16 v[98:113], v[98:101], v[130:133], 0
	s_waitcnt vmcnt(3)
	s_nop 9
	v_add_f32_e32 v1, v82, v4
	v_mfma_f32_32x32x16_f16 v[98:113], v[118:121], v[134:137], v[98:113]
	v_add_f32_e32 v3, v5, v83
	v_add_f32_e32 v4, v6, v84
	v_add_f32_e32 v5, v7, v85
	v_mul_f32_e32 v1, 0xbfb8aa3b, v1
	v_mul_f32_e32 v3, 0xbfb8aa3b, v3
	v_mul_f32_e32 v4, 0xbfb8aa3b, v4
	v_mul_f32_e32 v5, 0xbfb8aa3b, v5
	v_mfma_f32_32x32x16_f16 v[98:113], v[122:125], v[138:141], v[98:113]
	v_exp_f32_e32 v1, v1
	v_exp_f32_e32 v3, v3
	v_exp_f32_e32 v4, v4
	v_exp_f32_e32 v5, v5
	v_add_f32_e32 v1, 1.0, v1
	v_add_f32_e32 v3, 1.0, v3
	v_add_f32_e32 v4, 1.0, v4
	v_mfma_f32_32x32x16_f16 v[98:113], v[126:129], v[142:145], v[98:113]
	v_add_f32_e32 v5, 1.0, v5
	s_waitcnt vmcnt(2)
	v_add_f32_e32 v16, v116, v96
	v_add_f32_e32 v17, v117, v97
	v_mul_f32_e32 v16, 0xbfb8aa3b, v16
	v_mul_f32_e32 v17, 0xbfb8aa3b, v17
	v_exp_f32_e32 v16, v16
	v_exp_f32_e32 v17, v17
	v_mfma_f32_32x32x16_f16 v[98:113], v[196:199], v[146:149], v[98:113]
	s_waitcnt vmcnt(1)
	v_add_f32_e32 v6, v86, v8
	v_add_f32_e32 v7, v9, v87
	v_add_f32_e32 v8, v10, v88
	v_add_f32_e32 v9, v11, v89
	v_mul_f32_e32 v6, 0xbfb8aa3b, v6
	v_mul_f32_e32 v7, 0xbfb8aa3b, v7
	v_mul_f32_e32 v8, 0xbfb8aa3b, v8
	v_mfma_f32_32x32x16_f16 v[98:113], v[200:203], v[150:153], v[98:113]
	s_waitcnt vmcnt(0)
	v_add_f32_e32 v10, v90, v12
	v_add_f32_e32 v11, v13, v91
	v_add_f32_e32 v12, v14, v92
	v_add_f32_e32 v13, v15, v93
	v_add_f32_e32 v14, v94, v114
	v_add_f32_e32 v15, v115, v95
	v_mul_f32_e32 v9, 0xbfb8aa3b, v9
	v_mfma_f32_32x32x16_f16 v[98:113], v[230:233], v[154:157], v[98:113]
	v_mul_f32_e32 v10, 0xbfb8aa3b, v10
	v_mul_f32_e32 v11, 0xbfb8aa3b, v11
	v_mul_f32_e32 v12, 0xbfb8aa3b, v12
	v_mul_f32_e32 v13, 0xbfb8aa3b, v13
	v_mul_f32_e32 v14, 0xbfb8aa3b, v14
	v_mul_f32_e32 v15, 0xbfb8aa3b, v15
	v_exp_f32_e32 v6, v6
	v_exp_f32_e32 v7, v7
	v_exp_f32_e32 v8, v8
	v_exp_f32_e32 v9, v9
	v_exp_f32_e32 v10, v10
	v_exp_f32_e32 v11, v11
	v_exp_f32_e32 v12, v12
	v_exp_f32_e32 v13, v13
	v_exp_f32_e32 v14, v14
	v_exp_f32_e32 v15, v15
	v_mfma_f32_32x32x16_f16 v[98:113], v[236:239], v[158:161], v[98:113]
	v_add_f32_e32 v6, 1.0, v6
	v_add_f32_e32 v7, 1.0, v7
	v_add_f32_e32 v8, 1.0, v8
	v_add_f32_e32 v9, 1.0, v9
	v_add_f32_e32 v10, 1.0, v10
	v_add_f32_e32 v11, 1.0, v11
	v_add_f32_e32 v12, 1.0, v12
	v_add_f32_e32 v13, 1.0, v13
	v_add_f32_e32 v14, 1.0, v14
	v_add_f32_e32 v15, 1.0, v15
	v_add_f32_e32 v16, 1.0, v16
	v_add_f32_e32 v17, 1.0, v17
	v_rcp_f32_e32 v1, v1
	v_rcp_f32_e32 v3, v3
	v_rcp_f32_e32 v4, v4
	v_rcp_f32_e32 v5, v5
	v_rcp_f32_e32 v6, v6
	v_rcp_f32_e32 v7, v7
	v_rcp_f32_e32 v8, v8
	v_rcp_f32_e32 v9, v9
	v_rcp_f32_e32 v10, v10
	v_rcp_f32_e32 v11, v11
	v_rcp_f32_e32 v12, v12
	v_rcp_f32_e32 v13, v13
	v_rcp_f32_e32 v14, v14
	v_rcp_f32_e32 v15, v15
	v_rcp_f32_e32 v16, v16
	v_rcp_f32_e32 v17, v17
	v_cvt_pk_f16_f32 v228, v10, v11
	v_cvt_pk_f16_f32 v231, v12, v13
	v_cvt_pk_f16_f32 v233, v14, v15
	v_cvt_pk_f16_f32 v235, v16, v17
	v_cvt_pk_f16_f32 v229, v1, v3
	v_cvt_pk_f16_f32 v230, v4, v5
	v_cvt_pk_f16_f32 v232, v6, v7
	v_cvt_pk_f16_f32 v234, v8, v9
	v_cvt_pk_f16_f32 v202, v106, v107
	v_cvt_pk_f16_f32 v203, v108, v109
	v_cvt_pk_f16_f32 v204, v110, v111
	v_cvt_pk_f16_f32 v205, v112, v113
	v_cvt_pk_f16_f32 v198, v98, v99
	v_cvt_pk_f16_f32 v199, v100, v101
	v_cvt_pk_f16_f32 v200, v102, v103
	v_cvt_pk_f16_f32 v201, v104, v105
	s_branch .LBB1_5
.LBB1_61:
	ds_read_b128 v[4:7], v226
	ds_read_b128 v[8:11], v226 offset:16
	ds_read_b128 v[12:15], v206 offset:32768
	ds_read_b128 v[82:85], v226 offset:32
	ds_read_b128 v[86:89], v226 offset:48
	s_waitcnt lgkmcnt(3)
	v_fma_mix_f32 v66, v190, s42, v4 op_sel:[0,0,0] op_sel_hi:[1,0,0]
	v_fma_mix_f32 v67, v190, s42, v5 op_sel:[1,0,0] op_sel_hi:[1,0,0]
	v_fma_mix_f32 v68, v191, s42, v6 op_sel:[0,0,0] op_sel_hi:[1,0,0]
	v_fma_mix_f32 v69, v191, s42, v7 op_sel:[1,0,0] op_sel_hi:[1,0,0]
	v_fma_mix_f32 v70, v192, s42, v8 op_sel:[0,0,0] op_sel_hi:[1,0,0]
	v_fma_mix_f32 v71, v192, s42, v9 op_sel:[1,0,0] op_sel_hi:[1,0,0]
	v_fma_mix_f32 v72, v193, s42, v10 op_sel:[0,0,0] op_sel_hi:[1,0,0]
	v_fma_mix_f32 v73, v193, s42, v11 op_sel:[1,0,0] op_sel_hi:[1,0,0]
	ds_read_b128 v[4:7], v206 offset:33792
	s_waitcnt lgkmcnt(1)
	v_fma_mix_f32 v74, v186, s42, v82 op_sel:[0,0,0] op_sel_hi:[1,0,0]
	v_fma_mix_f32 v75, v186, s42, v83 op_sel:[1,0,0] op_sel_hi:[1,0,0]
	v_fma_mix_f32 v76, v187, s42, v84 op_sel:[0,0,0] op_sel_hi:[1,0,0]
	v_fma_mix_f32 v77, v187, s42, v85 op_sel:[1,0,0] op_sel_hi:[1,0,0]
	v_fma_mix_f32 v78, v188, s42, v86 op_sel:[0,0,0] op_sel_hi:[1,0,0]
	v_fma_mix_f32 v79, v188, s42, v87 op_sel:[1,0,0] op_sel_hi:[1,0,0]
	v_fma_mix_f32 v80, v189, s42, v88 op_sel:[0,0,0] op_sel_hi:[1,0,0]
	v_fma_mix_f32 v81, v189, s42, v89 op_sel:[1,0,0] op_sel_hi:[1,0,0]
	s_nop 1
	s_nop 0
	v_mfma_f32_32x32x16_f16 v[66:81], v[12:15], v[198:201], v[66:81]
	s_waitcnt lgkmcnt(0)
	v_mfma_f32_32x32x16_f16 v[66:81], v[4:7], v[202:205], v[66:81]
	v_cndmask_b32_e64 v1, 0, 1, s[0:1]
	v_cmp_ne_u32_e64 s[16:17], 1, v1
	s_andn2_b64 vcc, exec, s[0:1]
	s_cbranch_vccnz .LBB1_8
.LBB1_62:
	ds_read_b128 v[4:7], v226 offset:128
	ds_read_b128 v[8:11], v226 offset:144
	ds_read_b128 v[12:15], v206 offset:34816
	ds_read_b128 v[82:85], v226 offset:160
	ds_read_b128 v[86:89], v226 offset:176
	s_waitcnt lgkmcnt(3)
	v_fma_mix_f32 v50, v182, s42, v4 op_sel:[0,0,0] op_sel_hi:[1,0,0]
	v_fma_mix_f32 v51, v182, s42, v5 op_sel:[1,0,0] op_sel_hi:[1,0,0]
	v_fma_mix_f32 v52, v183, s42, v6 op_sel:[0,0,0] op_sel_hi:[1,0,0]
	v_fma_mix_f32 v53, v183, s42, v7 op_sel:[1,0,0] op_sel_hi:[1,0,0]
	v_fma_mix_f32 v54, v184, s42, v8 op_sel:[0,0,0] op_sel_hi:[1,0,0]
	v_fma_mix_f32 v55, v184, s42, v9 op_sel:[1,0,0] op_sel_hi:[1,0,0]
	v_fma_mix_f32 v56, v185, s42, v10 op_sel:[0,0,0] op_sel_hi:[1,0,0]
	v_fma_mix_f32 v57, v185, s42, v11 op_sel:[1,0,0] op_sel_hi:[1,0,0]
	ds_read_b128 v[4:7], v206 offset:35840
	s_waitcnt lgkmcnt(1)
	v_fma_mix_f32 v58, v178, s42, v82 op_sel:[0,0,0] op_sel_hi:[1,0,0]
	v_fma_mix_f32 v59, v178, s42, v83 op_sel:[1,0,0] op_sel_hi:[1,0,0]
	v_fma_mix_f32 v60, v179, s42, v84 op_sel:[0,0,0] op_sel_hi:[1,0,0]
	v_fma_mix_f32 v61, v179, s42, v85 op_sel:[1,0,0] op_sel_hi:[1,0,0]
	v_fma_mix_f32 v62, v180, s42, v86 op_sel:[0,0,0] op_sel_hi:[1,0,0]
	v_fma_mix_f32 v63, v180, s42, v87 op_sel:[1,0,0] op_sel_hi:[1,0,0]
	v_fma_mix_f32 v64, v181, s42, v88 op_sel:[0,0,0] op_sel_hi:[1,0,0]
	v_fma_mix_f32 v65, v181, s42, v89 op_sel:[1,0,0] op_sel_hi:[1,0,0]
	s_nop 1
	s_nop 0
	v_mfma_f32_32x32x16_f16 v[50:65], v[12:15], v[198:201], v[50:65]
	s_waitcnt lgkmcnt(0)
	v_mfma_f32_32x32x16_f16 v[50:65], v[4:7], v[202:205], v[50:65]
	v_cndmask_b32_e64 v1, 0, 1, s[6:7]
	v_cmp_ne_u32_e64 s[18:19], 1, v1
	s_andn2_b64 vcc, exec, s[6:7]
	s_cbranch_vccnz .LBB1_9
.LBB1_63:
	ds_read_b128 v[4:7], v226 offset:256
	ds_read_b128 v[8:11], v226 offset:272
	ds_read_b128 v[12:15], v206 offset:36864
	ds_read_b128 v[82:85], v226 offset:288
	ds_read_b128 v[86:89], v226 offset:304
	s_waitcnt lgkmcnt(3)
	v_fma_mix_f32 v34, v170, s42, v4 op_sel:[0,0,0] op_sel_hi:[1,0,0]
	v_fma_mix_f32 v35, v170, s42, v5 op_sel:[1,0,0] op_sel_hi:[1,0,0]
	v_fma_mix_f32 v36, v171, s42, v6 op_sel:[0,0,0] op_sel_hi:[1,0,0]
	v_fma_mix_f32 v37, v171, s42, v7 op_sel:[1,0,0] op_sel_hi:[1,0,0]
	v_fma_mix_f32 v38, v172, s42, v8 op_sel:[0,0,0] op_sel_hi:[1,0,0]
	v_fma_mix_f32 v39, v172, s42, v9 op_sel:[1,0,0] op_sel_hi:[1,0,0]
	v_fma_mix_f32 v40, v173, s42, v10 op_sel:[0,0,0] op_sel_hi:[1,0,0]
	v_fma_mix_f32 v41, v173, s42, v11 op_sel:[1,0,0] op_sel_hi:[1,0,0]
	ds_read_b128 v[4:7], v206 offset:37888
	s_waitcnt lgkmcnt(1)
	v_fma_mix_f32 v42, v174, s42, v82 op_sel:[0,0,0] op_sel_hi:[1,0,0]
	v_fma_mix_f32 v43, v174, s42, v83 op_sel:[1,0,0] op_sel_hi:[1,0,0]
	v_fma_mix_f32 v44, v175, s42, v84 op_sel:[0,0,0] op_sel_hi:[1,0,0]
	v_fma_mix_f32 v45, v175, s42, v85 op_sel:[1,0,0] op_sel_hi:[1,0,0]
	v_fma_mix_f32 v46, v176, s42, v86 op_sel:[0,0,0] op_sel_hi:[1,0,0]
	v_fma_mix_f32 v47, v176, s42, v87 op_sel:[1,0,0] op_sel_hi:[1,0,0]
	v_fma_mix_f32 v48, v177, s42, v88 op_sel:[0,0,0] op_sel_hi:[1,0,0]
	v_fma_mix_f32 v49, v177, s42, v89 op_sel:[1,0,0] op_sel_hi:[1,0,0]
	s_nop 1
	s_nop 0
	v_mfma_f32_32x32x16_f16 v[34:49], v[12:15], v[198:201], v[34:49]
	s_waitcnt lgkmcnt(0)
	v_mfma_f32_32x32x16_f16 v[34:49], v[4:7], v[202:205], v[34:49]
	v_cndmask_b32_e64 v1, 0, 1, s[4:5]
	v_cmp_ne_u32_e64 s[20:21], 1, v1
	s_andn2_b64 vcc, exec, s[4:5]
	s_cbranch_vccz .LBB1_10
	s_branch .LBB1_11

.LBB1_71:
	s_waitcnt vmcnt(4)
	ds_read_b128 v[4:7], v226 offset:512
	ds_read_b128 v[8:11], v226 offset:528
	ds_read_b128 v[12:15], v206 offset:40960
	ds_read_b128 v[114:117], v226 offset:544
	ds_read_b128 v[118:121], v226 offset:560
	s_waitcnt lgkmcnt(0)
	v_fma_mix_f32 v66, v190, s42, v4 op_sel:[0,0,0] op_sel_hi:[1,0,0]
	v_fma_mix_f32 v67, v190, s42, v5 op_sel:[1,0,0] op_sel_hi:[1,0,0]
	v_fma_mix_f32 v68, v191, s42, v6 op_sel:[0,0,0] op_sel_hi:[1,0,0]
	v_fma_mix_f32 v69, v191, s42, v7 op_sel:[1,0,0] op_sel_hi:[1,0,0]
	v_fma_mix_f32 v70, v192, s42, v8 op_sel:[0,0,0] op_sel_hi:[1,0,0]
	v_fma_mix_f32 v71, v192, s42, v9 op_sel:[1,0,0] op_sel_hi:[1,0,0]
	v_fma_mix_f32 v72, v193, s42, v10 op_sel:[0,0,0] op_sel_hi:[1,0,0]
	v_fma_mix_f32 v73, v193, s42, v11 op_sel:[1,0,0] op_sel_hi:[1,0,0]
	ds_read_b128 v[4:7], v206 offset:41984
	v_fma_mix_f32 v74, v186, s42, v114 op_sel:[0,0,0] op_sel_hi:[1,0,0]
	v_fma_mix_f32 v75, v186, s42, v115 op_sel:[1,0,0] op_sel_hi:[1,0,0]
	v_fma_mix_f32 v76, v187, s42, v116 op_sel:[0,0,0] op_sel_hi:[1,0,0]
	v_fma_mix_f32 v77, v187, s42, v117 op_sel:[1,0,0] op_sel_hi:[1,0,0]
	v_fma_mix_f32 v78, v188, s42, v118 op_sel:[0,0,0] op_sel_hi:[1,0,0]
	v_fma_mix_f32 v79, v188, s42, v119 op_sel:[1,0,0] op_sel_hi:[1,0,0]
	v_fma_mix_f32 v80, v189, s42, v120 op_sel:[0,0,0] op_sel_hi:[1,0,0]
	v_fma_mix_f32 v81, v189, s42, v121 op_sel:[1,0,0] op_sel_hi:[1,0,0]
	s_nop 1
	s_nop 0
	v_mfma_f32_32x32x16_f16 v[66:81], v[12:15], v[198:201], v[66:81]
	s_waitcnt lgkmcnt(0)
	v_mfma_f32_32x32x16_f16 v[66:81], v[4:7], v[202:205], v[66:81]
	v_cndmask_b32_e64 v1, 0, 1, s[8:9]
	v_cmp_ne_u32_e64 s[20:21], 1, v1
	s_andn2_b64 vcc, exec, s[8:9]
	s_cbranch_vccnz .LBB1_34
.LBB1_72:
	s_waitcnt vmcnt(4)
	ds_read_b128 v[4:7], v226 offset:640
	ds_read_b128 v[8:11], v226 offset:656
	ds_read_b128 v[12:15], v206 offset:43008
	ds_read_b128 v[114:117], v226 offset:672
	ds_read_b128 v[118:121], v226 offset:688
	s_waitcnt lgkmcnt(0)
	v_fma_mix_f32 v50, v182, s42, v4 op_sel:[0,0,0] op_sel_hi:[1,0,0]
	v_fma_mix_f32 v51, v182, s42, v5 op_sel:[1,0,0] op_sel_hi:[1,0,0]
	v_fma_mix_f32 v52, v183, s42, v6 op_sel:[0,0,0] op_sel_hi:[1,0,0]
	v_fma_mix_f32 v53, v183, s42, v7 op_sel:[1,0,0] op_sel_hi:[1,0,0]
	v_fma_mix_f32 v54, v184, s42, v8 op_sel:[0,0,0] op_sel_hi:[1,0,0]
	v_fma_mix_f32 v55, v184, s42, v9 op_sel:[1,0,0] op_sel_hi:[1,0,0]
	v_fma_mix_f32 v56, v185, s42, v10 op_sel:[0,0,0] op_sel_hi:[1,0,0]
	v_fma_mix_f32 v57, v185, s42, v11 op_sel:[1,0,0] op_sel_hi:[1,0,0]
	ds_read_b128 v[4:7], v206 offset:44032
	v_fma_mix_f32 v58, v178, s42, v114 op_sel:[0,0,0] op_sel_hi:[1,0,0]
	v_fma_mix_f32 v59, v178, s42, v115 op_sel:[1,0,0] op_sel_hi:[1,0,0]
	v_fma_mix_f32 v60, v179, s42, v116 op_sel:[0,0,0] op_sel_hi:[1,0,0]
	v_fma_mix_f32 v61, v179, s42, v117 op_sel:[1,0,0] op_sel_hi:[1,0,0]
	v_fma_mix_f32 v62, v180, s42, v118 op_sel:[0,0,0] op_sel_hi:[1,0,0]
	v_fma_mix_f32 v63, v180, s42, v119 op_sel:[1,0,0] op_sel_hi:[1,0,0]
	v_fma_mix_f32 v64, v181, s42, v120 op_sel:[0,0,0] op_sel_hi:[1,0,0]
	v_fma_mix_f32 v65, v181, s42, v121 op_sel:[1,0,0] op_sel_hi:[1,0,0]
	s_nop 1
	s_nop 0
	v_mfma_f32_32x32x16_f16 v[50:65], v[12:15], v[198:201], v[50:65]
	s_waitcnt lgkmcnt(0)
	v_mfma_f32_32x32x16_f16 v[50:65], v[4:7], v[202:205], v[50:65]
	v_cndmask_b32_e64 v1, 0, 1, s[14:15]
	v_cmp_ne_u32_e64 s[22:23], 1, v1
	s_andn2_b64 vcc, exec, s[14:15]
	s_cbranch_vccnz .LBB1_35
.LBB1_73:
	s_waitcnt vmcnt(4)
	ds_read_b128 v[4:7], v226 offset:768
	ds_read_b128 v[8:11], v226 offset:784
	ds_read_b128 v[12:15], v206 offset:45056
	ds_read_b128 v[114:117], v226 offset:800
	ds_read_b128 v[118:121], v226 offset:816
	s_waitcnt lgkmcnt(0)
	v_fma_mix_f32 v34, v170, s42, v4 op_sel:[0,0,0] op_sel_hi:[1,0,0]
	v_fma_mix_f32 v35, v170, s42, v5 op_sel:[1,0,0] op_sel_hi:[1,0,0]
	v_fma_mix_f32 v36, v171, s42, v6 op_sel:[0,0,0] op_sel_hi:[1,0,0]
	v_fma_mix_f32 v37, v171, s42, v7 op_sel:[1,0,0] op_sel_hi:[1,0,0]
	v_fma_mix_f32 v38, v172, s42, v8 op_sel:[0,0,0] op_sel_hi:[1,0,0]
	v_fma_mix_f32 v39, v172, s42, v9 op_sel:[1,0,0] op_sel_hi:[1,0,0]
	v_fma_mix_f32 v40, v173, s42, v10 op_sel:[0,0,0] op_sel_hi:[1,0,0]
	v_fma_mix_f32 v41, v173, s42, v11 op_sel:[1,0,0] op_sel_hi:[1,0,0]
	ds_read_b128 v[4:7], v206 offset:46080
	v_fma_mix_f32 v42, v174, s42, v114 op_sel:[0,0,0] op_sel_hi:[1,0,0]
	v_fma_mix_f32 v43, v174, s42, v115 op_sel:[1,0,0] op_sel_hi:[1,0,0]
	v_fma_mix_f32 v44, v175, s42, v116 op_sel:[0,0,0] op_sel_hi:[1,0,0]
	v_fma_mix_f32 v45, v175, s42, v117 op_sel:[1,0,0] op_sel_hi:[1,0,0]
	v_fma_mix_f32 v46, v176, s42, v118 op_sel:[0,0,0] op_sel_hi:[1,0,0]
	v_fma_mix_f32 v47, v176, s42, v119 op_sel:[1,0,0] op_sel_hi:[1,0,0]
	v_fma_mix_f32 v48, v177, s42, v120 op_sel:[0,0,0] op_sel_hi:[1,0,0]
	v_fma_mix_f32 v49, v177, s42, v121 op_sel:[1,0,0] op_sel_hi:[1,0,0]
	s_nop 1
	s_nop 0
	v_mfma_f32_32x32x16_f16 v[34:49], v[12:15], v[198:201], v[34:49]
	s_waitcnt lgkmcnt(0)
	v_mfma_f32_32x32x16_f16 v[34:49], v[4:7], v[202:205], v[34:49]
	v_cndmask_b32_e64 v1, 0, 1, s[12:13]
	v_cmp_ne_u32_e64 s[24:25], 1, v1
	s_andn2_b64 vcc, exec, s[12:13]
	s_cbranch_vccnz .LBB1_36
.LBB1_74:
	s_waitcnt vmcnt(4)
	ds_read_b128 v[4:7], v226 offset:896
	ds_read_b128 v[8:11], v226 offset:912
	ds_read_b128 v[12:15], v206 offset:47104
	ds_read_b128 v[114:117], v226 offset:928
	ds_read_b128 v[118:121], v226 offset:944
	s_waitcnt lgkmcnt(0)
	v_fma_mix_f32 v18, v162, s42, v4 op_sel:[0,0,0] op_sel_hi:[1,0,0]
	v_fma_mix_f32 v19, v162, s42, v5 op_sel:[1,0,0] op_sel_hi:[1,0,0]
	v_fma_mix_f32 v20, v163, s42, v6 op_sel:[0,0,0] op_sel_hi:[1,0,0]
	v_fma_mix_f32 v21, v163, s42, v7 op_sel:[1,0,0] op_sel_hi:[1,0,0]
	v_fma_mix_f32 v22, v164, s42, v8 op_sel:[0,0,0] op_sel_hi:[1,0,0]
	v_fma_mix_f32 v23, v164, s42, v9 op_sel:[1,0,0] op_sel_hi:[1,0,0]
	v_fma_mix_f32 v24, v165, s42, v10 op_sel:[0,0,0] op_sel_hi:[1,0,0]
	v_fma_mix_f32 v25, v165, s42, v11 op_sel:[1,0,0] op_sel_hi:[1,0,0]
	ds_read_b128 v[4:7], v206 offset:48128
	v_fma_mix_f32 v26, v166, s42, v114 op_sel:[0,0,0] op_sel_hi:[1,0,0]
	v_fma_mix_f32 v27, v166, s42, v115 op_sel:[1,0,0] op_sel_hi:[1,0,0]
	v_fma_mix_f32 v28, v167, s42, v116 op_sel:[0,0,0] op_sel_hi:[1,0,0]
	v_fma_mix_f32 v29, v167, s42, v117 op_sel:[1,0,0] op_sel_hi:[1,0,0]
	v_fma_mix_f32 v30, v168, s42, v118 op_sel:[0,0,0] op_sel_hi:[1,0,0]
	v_fma_mix_f32 v31, v168, s42, v119 op_sel:[1,0,0] op_sel_hi:[1,0,0]
	v_fma_mix_f32 v32, v169, s42, v120 op_sel:[0,0,0] op_sel_hi:[1,0,0]
	v_fma_mix_f32 v33, v169, s42, v121 op_sel:[1,0,0] op_sel_hi:[1,0,0]
	s_nop 1
	s_nop 0
	v_mfma_f32_32x32x16_f16 v[18:33], v[12:15], v[198:201], v[18:33]
	s_waitcnt lgkmcnt(0)
	v_mfma_f32_32x32x16_f16 v[18:33], v[4:7], v[202:205], v[18:33]
	v_cndmask_b32_e64 v1, 0, 1, s[52:53]
	v_cmp_ne_u32_e64 s[16:17], 1, v1
	s_andn2_b64 vcc, exec, s[52:53]
	s_cbranch_vccz .LBB1_37
	s_branch .LBB1_38
